# combine-phase parameter staging: both iterations' loads issued up front, one wait (was 2-4 serialized round trips)
# baseline (speedup 1.0000x reference)
; #define GAS __attribute__((address_space(1)))
; #define LAS __attribute__((address_space(3)))
; __device__ __forceinline__ void phase_combine(Frame& F, int l) {
;     ...
;     LAS float* PV = (LAS float*)F.lds;
;     for (int i = F.tid; i < 4 * 256; i += NTHR) { const int b = i >> 8, c4 = i & 255; const GAS float* mb = modl + (size_t)b * 6144;
;         const f32x4 gf = ((const GAS f32x4*)(mb + 5120))[c4], pg = ((const GAS f32x4*)(INP(F, I_FPOST) + l * DM))[c4];
;         LAS f32x4* pv = (LAS f32x4*)(PV + b * 3072) + ((c4 >> 2) + 64 * (c4 & 3)); pv[0] = gf * pg;
;         if (l + 1 < DEPTH) { const GAS float* mn = modl + 4 * 6144 + (size_t)b * 6144; const f32x4 gg = ((const GAS f32x4*)(INP(F, I_MPRE) + (l + 1) * DM))[c4], s1 = ((const GAS f32x4*)(mn + 1024))[c4], s0 = ((const GAS f32x4*)mn)[c4];
;             pv[256] = gg * (1.0f + s1); pv[512] = s0; } }
;     __syncthreads();
.LBB0_1950:
	v_mov_b32_e32 v1, v0
	s_movk_i32 s0, 0x400
	s_nop 0
	v_readfirstlane_b32 s14, v1
	v_cmp_gt_i32_e32 vcc, s0, v1
	s_and_saveexec_b64 s[0:1], vcc
	s_movk_i32 s18, 0x1ff
	s_cbranch_execz .LBB0_1956
	s_mul_i32 s94, s54, 0x6000
	s_lshl_b64 s[2:3], s[94:95], 2
	s_add_u32 s6, s58, s2
	s_addc_u32 s7, s59, s3
	s_add_u32 s2, s6, 0x100000
	s_addc_u32 s3, s7, 0
	s_lshl_b32 s94, s54, 10
	v_lshlrev_b32_e32 v3, 2, v1
	s_add_u32 s6, s6, 0x118000
	v_and_b32_e32 v3, 0x3f0, v3
	s_addc_u32 s7, s7, 0
	v_and_b32_e32 v2, 0xff, v1
	v_add_u32_e32 v3, 0, v3
	s_waitcnt vmcnt(0)
	v_lshlrev_b32_e32 v6, 6, v1
	s_mov_b64 s[8:9], 0
	s_lshl_b64 s[10:11], s[94:95], 2
	v_mov_b32_e32 v7, v1
	v_ashrrev_i32_e32 v18, 8, v7
	v_mul_i32_i24_e32 v4, 0x1800, v18
	v_mov_b32_e32 v5, 0
	v_lshlrev_b32_e32 v182, 4, v2
	v_lshl_add_u64 v[8:9], v[4:5], 2, s[2:3]
	v_lshl_add_u64 v[8:9], v[8:9], 0, v[182:183]
	v_add_co_u32_e32 v8, vcc, 0x5000, v8
	s_nop 1
	v_addc_co_u32_e32 v9, vcc, 0, v9, vcc
	global_load_dwordx4 v[10:13], v[8:9], off
	v_add_co_u32_e32 v212, vcc, 0xc000, v8
	s_nop 1
	v_addc_co_u32_e32 v213, vcc, 0, v9, vcc
	global_load_dwordx4 v[188:191], v[212:213], off
	v_mov_b32_e32 v8, s19
	ds_read_b64 v[8:9], v8
	s_waitcnt lgkmcnt(0)
	v_readfirstlane_b32 s15, v8
	v_readfirstlane_b32 s17, v9
	s_add_u32 s16, s15, s10
	s_addc_u32 s17, s17, s11
	v_and_b32_e32 v9, 0xc0, v6
	v_mul_i32_i24_e32 v8, 0x3000, v18
	v_lshlrev_b32_e32 v9, 4, v9
	global_load_dwordx4 v[14:17], v182, s[16:17]
	v_readlane_b32 s16, v254, 57
	v_readlane_b32 s17, v254, 58
	v_add3_u32 v8, v3, v8, v9
	s_andn2_b64 vcc, exec, s[16:17]
	s_cbranch_vccnz .Ljs_nonext
	v_mov_b32_e32 v9, s20
	ds_read_b64 v[212:213], v9
	v_lshl_add_u64 v[4:5], v[4:5], 2, s[6:7]
	v_lshl_add_u64 v[4:5], v[4:5], 0, v[182:183]
	s_waitcnt lgkmcnt(0)
	v_readfirstlane_b32 s16, v212
	v_readfirstlane_b32 s17, v213
	s_nop 1
	v_lshl_add_u64 v[212:213], s[16:17], 0, v[182:183]
	v_add_co_u32_e32 v212, vcc, 0x1000, v212
	s_nop 1
	v_addc_co_u32_e32 v213, vcc, 0, v213, vcc
	global_load_dwordx4 v[192:195], v[212:213], off
	v_add_co_u32_e32 v212, vcc, 0x1000, v4
	s_nop 1
	v_addc_co_u32_e32 v213, vcc, 0, v5, vcc
	global_load_dwordx4 v[196:199], v[212:213], off
	global_load_dwordx4 v[200:203], v[4:5], off
	v_add_co_u32_e32 v212, vcc, 0xd000, v4
	s_nop 1
	v_addc_co_u32_e32 v213, vcc, 0, v5, vcc
	global_load_dwordx4 v[204:207], v[212:213], off
	v_add_co_u32_e32 v212, vcc, 0xc000, v4
	s_nop 1
	v_addc_co_u32_e32 v213, vcc, 0, v5, vcc
	global_load_dwordx4 v[208:211], v[212:213], off
	s_waitcnt vmcnt(0)
	v_pk_add_f32 v[196:197], v[196:197], 1.0 op_sel_hi:[1,0]
	v_pk_add_f32 v[198:199], v[198:199], 1.0 op_sel_hi:[1,0]
	v_pk_add_f32 v[204:205], v[204:205], 1.0 op_sel_hi:[1,0]
	v_pk_add_f32 v[206:207], v[206:207], 1.0 op_sel_hi:[1,0]
	v_pk_mul_f32 v[196:197], v[192:193], v[196:197]
	v_pk_mul_f32 v[198:199], v[194:195], v[198:199]
	v_pk_mul_f32 v[204:205], v[192:193], v[204:205]
	v_pk_mul_f32 v[206:207], v[194:195], v[206:207]
	ds_write_b128 v8, v[196:199] offset:4096
	ds_write_b128 v8, v[200:203] offset:8192
	ds_write_b128 v8, v[204:207] offset:28672
	ds_write_b128 v8, v[208:211] offset:32768
.Ljs_nonext:
	s_waitcnt vmcnt(0)
	v_pk_mul_f32 v[12:13], v[12:13], v[16:17]
	v_pk_mul_f32 v[10:11], v[10:11], v[14:15]
	v_pk_mul_f32 v[190:191], v[190:191], v[16:17]
	v_pk_mul_f32 v[188:189], v[188:189], v[14:15]
	ds_write_b128 v8, v[10:13]
	ds_write_b128 v8, v[188:191] offset:24576
	v_add_u32_e32 v7, 0x400, v7
	v_add_u32_e32 v6, 0x10000, v6
	s_branch .LBB0_1956
